# stack19
# speedup vs baseline: 1.0176x; 1.0026x over previous
.LBB3_17:
	s_lshl_b32 s19, s30, 16
	s_and_b32 s19, s19, 0x10000
	s_or_b32 s8, s8, s33
	s_and_b64 vcc, exec, s[26:27]
	s_cbranch_vccz .LBB3_19
	s_add_i32 s26, s44, s8
	v_lshl_add_u32 v70, v0, 4, s19
	ds_read_b128 v[74:77], v70
	ds_read_b128 v[78:81], v70 offset:8192
	ds_read_b128 v[82:85], v70 offset:16384
	ds_read_b128 v[86:89], v70 offset:24576
	ds_read_b128 v[90:93], v70 offset:32768
	ds_read_b128 v[94:97], v70 offset:40960
	ds_read_b128 v[98:101], v70 offset:49152
	ds_read_b128 v[240:243], v70 offset:57344
	s_ashr_i32 s27, s26, 31
	s_lshl_b64 s[26:27], s[26:27], 16
	s_add_u32 s26, s6, s26
	s_addc_u32 s27, s7, s27
	v_lshl_add_u64 v[66:67], s[26:27], 0, v[102:103]
	s_waitcnt lgkmcnt(7)
	global_store_dwordx4 v102, v[74:77], s[26:27]
	v_add_co_u32_e32 v68, vcc, s64, v66
	s_nop 0
	v_addc_co_u32_e32 v69, vcc, 0, v67, vcc
	s_waitcnt lgkmcnt(6)
	global_store_dwordx4 v[68:69], v[78:81], off
	v_lshlrev_b32_e32 v68, 4, v1
	s_waitcnt lgkmcnt(5)
	global_store_dwordx4 v68, v[82:85], s[26:27]
	v_add_co_u32_e32 v68, vcc, s65, v66
	s_nop 0
	v_addc_co_u32_e32 v69, vcc, 0, v67, vcc
	s_waitcnt lgkmcnt(4)
	global_store_dwordx4 v[68:69], v[86:89], off
	v_lshlrev_b32_e32 v68, 4, v165
	s_waitcnt lgkmcnt(3)
	global_store_dwordx4 v68, v[90:93], s[26:27]
	v_add_co_u32_e32 v68, vcc, s66, v66
	s_nop 0
	v_addc_co_u32_e32 v69, vcc, 0, v67, vcc
	s_waitcnt lgkmcnt(2)
	global_store_dwordx4 v[68:69], v[94:97], off
	v_lshlrev_b32_e32 v68, 4, v232
	s_waitcnt lgkmcnt(1)
	global_store_dwordx4 v68, v[98:101], s[26:27]
	s_andn2_b64 s[24:25], s[24:25], exec
	s_and_b64 s[26:27], s[2:3], exec
	v_add_co_u32_e32 v58, vcc, 0xe000, v66
	s_or_b64 s[24:25], s[24:25], s[26:27]
	s_nop 0
	v_addc_co_u32_e32 v59, vcc, 0, v67, vcc
	s_waitcnt lgkmcnt(0)
	global_store_dwordx4 v[58:59], v[240:243], off
	v_mov_b32_e32 v58, v230
